# speedup vs baseline: 1.0145x; 1.0145x over previous
.LBB0_32:
	s_or_b64 exec, exec, s[2:3]
	v_mov_b32_e32 v2, s8
	v_lshrrev_b32_e32 v106, 4, v1
	ds_read_b128 v[4:7], v2
	v_lshl_add_u32 v2, v106, 2, s7
	ds_read2_b32 v[14:15], v2 offset1:4
	v_mov_b32_e32 v2, 0
	v_cmp_ne_u32_e64 s[16:17], 3, v106
	s_waitcnt lgkmcnt(0)
	v_readfirstlane_b32 s35, v4
	v_readfirstlane_b32 s36, v5
	v_mov_b32_e32 v3, v2
	v_mov_b32_e32 v4, v2
	v_mov_b32_e32 v5, v2
	v_lshlrev_b32_e32 v107, 4, v82
	s_and_saveexec_b64 s[4:5], s[16:17]
	s_cbranch_execz .LBB0_34
	v_mov_b32_e32 v3, s8
	ds_read_b32 v3, v3 offset:16
	v_mov_b32_e32 v4, s14
	v_mov_b32_e32 v5, s26
	v_cmp_eq_u32_e32 vcc, 1, v106
	v_mov_b32_e32 v8, s27
	v_cmp_gt_u32_e64 s[2:3], 16, v1
	v_cndmask_b32_e32 v4, v4, v5, vcc
	v_mov_b32_e32 v5, s15
	v_cndmask_b32_e32 v5, v5, v8, vcc
	v_mov_b32_e32 v8, s25
	s_waitcnt lgkmcnt(0)
	v_cndmask_b32_e32 v3, v3, v7, vcc
	v_cndmask_b32_e64 v5, v5, v8, s[2:3]
	v_mov_b32_e32 v8, s24
	v_cndmask_b32_e64 v3, v3, v6, s[2:3]
	v_lshlrev_b32_e32 v6, 4, v82
	v_cndmask_b32_e64 v4, v4, v8, s[2:3]
	v_lshl_or_b32 v6, v3, 8, v6
	v_mov_b32_e32 v7, v2
	v_lshl_add_u64 v[2:3], v[4:5], 0, v[6:7]
	global_load_dwordx4 v[2:5], v[2:3], off sc0 nt

.LBB0_40:
	s_or_b64 exec, exec, s[2:3]
	v_and_b32_e32 v83, 48, v0
	v_lshl_add_u32 v64, v83, 2, s6
	ds_read_b128 v[28:31], v64
	v_mov_b32_e32 v18, 0
	v_mov_b32_e32 v19, v18
	v_mov_b32_e32 v20, v18
	v_mov_b32_e32 v21, v18
	v_mov_b64_e32 v[14:15], v[18:19]
	v_cmp_gt_i32_e32 vcc, s35, v106
	v_mov_b64_e32 v[16:17], v[20:21]
	s_and_saveexec_b64 s[2:3], vcc
	s_cbranch_execz .LBB0_42
	s_waitcnt lgkmcnt(0)
	v_lshl_or_b32 v14, v28, 8, v107
	global_load_dwordx4 v[14:17], v14, s[28:29] sc0 nt
.LBB0_42:
	s_or_b64 exec, exec, s[2:3]
	s_add_i32 s2, s35, -4
	v_cmp_gt_i32_e32 vcc, s2, v106
	s_and_saveexec_b64 s[2:3], vcc
	s_cbranch_execz .LBB0_44
	s_waitcnt lgkmcnt(0)
	v_lshl_or_b32 v18, v29, 8, v107
	global_load_dwordx4 v[18:21], v18, s[28:29] sc0 nt
.LBB0_44:
	s_or_b64 exec, exec, s[2:3]
	v_mov_b32_e32 v26, 0
	v_mov_b32_e32 v27, v26
	s_add_i32 s2, s35, -8
	s_waitcnt lgkmcnt(0)
	v_mov_b32_e32 v28, v26
	v_mov_b32_e32 v29, v26
	v_mov_b64_e32 v[22:23], v[26:27]
	v_cmp_gt_i32_e32 vcc, s2, v106
	v_mov_b64_e32 v[24:25], v[28:29]
	s_and_saveexec_b64 s[2:3], vcc
	s_cbranch_execz .LBB0_46
	v_lshl_or_b32 v22, v30, 8, v107
	global_load_dwordx4 v[22:25], v22, s[28:29] sc0 nt
.LBB0_46:
	s_or_b64 exec, exec, s[2:3]
	s_add_i32 s2, s35, -12
	v_cmp_gt_i32_e32 vcc, s2, v106
	s_and_saveexec_b64 s[2:3], vcc
	s_cbranch_execz .LBB0_48
	v_lshl_or_b32 v26, v31, 8, v107
	global_load_dwordx4 v[26:29], v26, s[28:29] sc0 nt
.LBB0_48:
	s_or_b64 exec, exec, s[2:3]
	ds_read_b128 v[44:47], v64 offset:16
	v_mov_b32_e32 v34, 0
	v_mov_b32_e32 v35, v34
	s_add_i32 s2, s35, -16
	v_mov_b32_e32 v36, v34
	v_mov_b32_e32 v37, v34
	v_mov_b64_e32 v[30:31], v[34:35]
	v_cmp_gt_i32_e32 vcc, s2, v106
	v_mov_b64_e32 v[32:33], v[36:37]
	s_and_saveexec_b64 s[2:3], vcc
	s_cbranch_execz .LBB0_50
	s_waitcnt lgkmcnt(0)
	v_lshl_or_b32 v30, v44, 8, v107
	global_load_dwordx4 v[30:33], v30, s[28:29] sc0 nt
.LBB0_50:
	s_or_b64 exec, exec, s[2:3]
	s_sub_i32 s2, s35, 20
	v_cmp_gt_i32_e32 vcc, s2, v106
	s_and_saveexec_b64 s[2:3], vcc
	s_cbranch_execz .LBB0_52
	s_waitcnt lgkmcnt(0)
	v_lshl_or_b32 v34, v45, 8, v107
	global_load_dwordx4 v[34:37], v34, s[28:29] sc0 nt
.LBB0_52:
	s_or_b64 exec, exec, s[2:3]
	v_mov_b32_e32 v42, 0
	v_mov_b32_e32 v43, v42
	s_sub_i32 s2, s35, 24
	s_waitcnt lgkmcnt(0)
	v_mov_b32_e32 v44, v42
	v_mov_b32_e32 v45, v42
	v_mov_b64_e32 v[38:39], v[42:43]
	v_cmp_gt_i32_e32 vcc, s2, v106
	v_mov_b64_e32 v[40:41], v[44:45]
	s_and_saveexec_b64 s[2:3], vcc
	s_cbranch_execz .LBB0_54
	v_lshl_or_b32 v38, v46, 8, v107
	global_load_dwordx4 v[38:41], v38, s[28:29] sc0 nt
.LBB0_54:
	s_or_b64 exec, exec, s[2:3]
	s_sub_i32 s2, s35, 28
	v_cmp_gt_i32_e32 vcc, s2, v106
	s_and_saveexec_b64 s[2:3], vcc
	s_cbranch_execz .LBB0_56
	v_lshl_or_b32 v42, v47, 8, v107
	global_load_dwordx4 v[42:45], v42, s[28:29] sc0 nt
.LBB0_56:
	s_or_b64 exec, exec, s[2:3]
	ds_read_b128 v[60:63], v64 offset:32
	v_mov_b32_e32 v50, 0
	v_mov_b32_e32 v51, v50
	s_sub_i32 s2, s35, 32
	v_mov_b32_e32 v52, v50
	v_mov_b32_e32 v53, v50
	v_mov_b64_e32 v[46:47], v[50:51]
	v_cmp_gt_i32_e32 vcc, s2, v106
	v_mov_b64_e32 v[48:49], v[52:53]
	s_and_saveexec_b64 s[2:3], vcc
	s_cbranch_execz .LBB0_58
	s_waitcnt lgkmcnt(0)
	v_lshl_or_b32 v46, v60, 8, v107
	global_load_dwordx4 v[46:49], v46, s[28:29] sc0 nt
.LBB0_58:
	s_or_b64 exec, exec, s[2:3]
	s_sub_i32 s2, s35, 36
	v_cmp_gt_i32_e32 vcc, s2, v106
	s_and_saveexec_b64 s[2:3], vcc
	s_cbranch_execz .LBB0_60
	s_waitcnt lgkmcnt(0)
	v_lshl_or_b32 v50, v61, 8, v107
	global_load_dwordx4 v[50:53], v50, s[28:29] sc0 nt
.LBB0_60:
	s_or_b64 exec, exec, s[2:3]
	v_mov_b32_e32 v58, 0
	v_mov_b32_e32 v59, v58
	s_sub_i32 s2, s35, 40
	s_waitcnt lgkmcnt(0)
	v_mov_b32_e32 v60, v58
	v_mov_b32_e32 v61, v58
	v_mov_b64_e32 v[54:55], v[58:59]
	v_cmp_gt_i32_e32 vcc, s2, v106
	v_mov_b64_e32 v[56:57], v[60:61]
	s_and_saveexec_b64 s[2:3], vcc
	s_cbranch_execz .LBB0_62
	v_lshl_or_b32 v54, v62, 8, v107
	global_load_dwordx4 v[54:57], v54, s[28:29] sc0 nt
.LBB0_62:
	s_or_b64 exec, exec, s[2:3]
	s_sub_i32 s2, s35, 44
	v_cmp_gt_i32_e32 vcc, s2, v106
	s_and_saveexec_b64 s[2:3], vcc
	s_cbranch_execz .LBB0_64
	v_lshl_or_b32 v58, v63, 8, v107
	global_load_dwordx4 v[58:61], v58, s[28:29] sc0 nt
.LBB0_64:
	s_or_b64 exec, exec, s[2:3]
	ds_read_b128 v[62:65], v64 offset:48
	v_mov_b32_e32 v70, 0
	v_mov_b32_e32 v71, v70
	s_sub_i32 s2, s35, 48
	v_mov_b32_e32 v72, v70
	v_mov_b32_e32 v73, v70
	v_mov_b64_e32 v[66:67], v[70:71]
	v_cmp_gt_i32_e32 vcc, s2, v106
	v_mov_b64_e32 v[68:69], v[72:73]
	s_and_saveexec_b64 s[2:3], vcc
	s_cbranch_execz .LBB0_66
	s_waitcnt lgkmcnt(0)
	v_lshl_or_b32 v62, v62, 8, v107
	global_load_dwordx4 v[66:69], v62, s[28:29] sc0 nt
.LBB0_66:
	s_or_b64 exec, exec, s[2:3]
	s_sub_i32 s2, s35, 52
	v_cmp_gt_i32_e32 vcc, s2, v106
	s_and_saveexec_b64 s[2:3], vcc
	s_cbranch_execz .LBB0_68
	s_waitcnt lgkmcnt(0)
	v_lshl_or_b32 v62, v63, 8, v107
	global_load_dwordx4 v[70:73], v62, s[28:29] sc0 nt
.LBB0_68:
	s_or_b64 exec, exec, s[2:3]
	v_mov_b32_e32 v78, 0
	v_mov_b32_e32 v79, v78
	s_sub_i32 s2, s35, 56
	v_mov_b32_e32 v80, v78
	v_mov_b32_e32 v81, v78
	v_mov_b64_e32 v[74:75], v[78:79]
	v_cmp_gt_i32_e32 vcc, s2, v106
	v_mov_b64_e32 v[76:77], v[80:81]
	s_and_saveexec_b64 s[2:3], vcc
	s_cbranch_execz .LBB0_70
	s_waitcnt lgkmcnt(0)
	v_lshl_or_b32 v62, v64, 8, v107
	global_load_dwordx4 v[74:77], v62, s[28:29] sc0 nt
.LBB0_70:
	s_or_b64 exec, exec, s[2:3]
	s_mov_b64 s[20:21], s[84:85]
	s_mov_b64 s[22:23], s[86:87]
	s_sub_i32 s0, s35, 60
	v_cmp_gt_i32_e32 vcc, s0, v106
	s_and_saveexec_b64 s[0:1], vcc
	s_cbranch_execz .LBB0_72
	s_waitcnt lgkmcnt(0)
	v_lshl_or_b32 v62, v65, 8, v107
	global_load_dwordx4 v[78:81], v62, s[28:29] sc0 nt

.LBB0_78:
	s_or_b64 exec, exec, s[0:1]
	v_readfirstlane_b32 s0, v63
	s_lshl_b32 s1, s0, 2
	s_waitcnt vmcnt(0)
	v_pk_add_f32 v[82:83], v[16:17], v[20:21]
	v_pk_add_f32 v[84:85], v[14:15], v[18:19]
	s_waitcnt vmcnt(0)
	v_pk_add_f32 v[88:89], v[24:25], v[28:29]
	v_pk_add_f32 v[90:91], v[22:23], v[26:27]
	s_and_b32 s1, s1, 60
	s_ashr_i32 s24, s0, 4
	v_pk_add_f32 v[82:83], v[82:83], v[88:89]
	v_pk_add_f32 v[84:85], v[84:85], v[90:91]
	v_pk_add_f32 v[88:89], v[32:33], v[36:37]
	v_pk_add_f32 v[90:91], v[30:31], v[34:35]
	v_pk_add_f32 v[92:93], v[40:41], v[44:45]
	v_pk_add_f32 v[94:95], v[38:39], v[42:43]
	s_add_i32 s24, s24, s1
	v_pk_add_f32 v[88:89], v[88:89], v[92:93]
	v_pk_add_f32 v[90:91], v[90:91], v[94:95]
	v_pk_add_f32 v[92:93], v[48:49], v[52:53]
	v_pk_add_f32 v[94:95], v[46:47], v[50:51]
	v_pk_add_f32 v[96:97], v[56:57], v[60:61]
	v_pk_add_f32 v[98:99], v[54:55], v[58:59]
	s_add_i32 s24, s24, 1
	v_pk_add_f32 v[92:93], v[92:93], v[96:97]
	v_pk_add_f32 v[94:95], v[94:95], v[98:99]
	v_pk_add_f32 v[96:97], v[68:69], v[72:73]
	v_pk_add_f32 v[98:99], v[66:67], v[70:71]
	v_pk_add_f32 v[100:101], v[76:77], v[80:81]
	v_pk_add_f32 v[102:103], v[74:75], v[78:79]
	s_cmp_lt_i32 s0, 48
	v_pk_add_f32 v[96:97], v[96:97], v[100:101]
	v_pk_add_f32 v[98:99], v[98:99], v[102:103]
	s_mul_i32 s0, s34, 0x110
	v_add_u32_e32 v63, 0xb000, v107
	v_pk_add_f32 v[86:87], v[6:7], v[10:11]
	v_pk_add_f32 v[82:83], v[82:83], v[88:89]
	v_pk_add_f32 v[84:85], v[84:85], v[90:91]
	v_pk_add_f32 v[88:89], v[92:93], v[96:97]
	v_pk_add_f32 v[90:91], v[94:95], v[98:99]
	v_add_u32_e32 v63, s0, v63
	v_pk_add_f32 v[88:89], v[82:83], v[88:89]
	v_pk_add_f32 v[98:99], v[84:85], v[90:91]
	ds_read_b128 v[82:85], v63
	v_mov_b32_e32 v63, v86
	s_nop 1
	v_permlane16_swap_b32_e32 v86, v63
	v_add_f32_e32 v90, v86, v63
	v_mov_b32_e32 v63, v87
	v_pk_add_f32 v[64:65], v[8:9], v[12:13]
	s_nop 0
	v_permlane16_swap_b32_e32 v87, v63
	v_add_f32_e32 v91, v87, v63
	v_mov_b32_e32 v63, v64
	s_nop 1
	v_permlane16_swap_b32_e32 v64, v63
	v_add_f32_e32 v94, v64, v63
	v_mov_b32_e32 v63, v65
	s_nop 1
	v_permlane16_swap_b32_e32 v65, v63
	v_add_f32_e32 v95, v65, v63
	v_mov_b32_e32 v63, v98
	s_nop 1
	v_permlane16_swap_b32_e32 v98, v63
	v_add_f32_e32 v98, v98, v63
	v_mov_b32_e32 v63, v99
	s_nop 1
	v_permlane16_swap_b32_e32 v99, v63
	v_add_f32_e32 v99, v99, v63
	v_mov_b32_e32 v63, v88
	s_nop 1
	v_permlane16_swap_b32_e32 v88, v63
	v_add_f32_e32 v102, v88, v63
	v_mov_b32_e32 v63, v89
	ds_bpermute_b32 v118, v108, v2
	ds_bpermute_b32 v115, v108, v3
	ds_bpermute_b32 v114, v108, v4
	ds_bpermute_b32 v127, v108, v5
	ds_bpermute_b32 v124, v109, v2
	ds_bpermute_b32 v126, v109, v3
	ds_bpermute_b32 v125, v109, v4
	ds_bpermute_b32 v123, v109, v5
	ds_bpermute_b32 v120, v110, v2
	ds_bpermute_b32 v122, v110, v3
	ds_bpermute_b32 v121, v110, v4
	ds_bpermute_b32 v119, v110, v5
	v_permlane16_swap_b32_e32 v89, v63
	v_add_f32_e32 v103, v89, v63
	v_mov_b32_e32 v92, v90
	v_mov_b32_e32 v93, v91
	v_mov_b32_e32 v96, v94
	v_mov_b32_e32 v97, v95
	v_mov_b32_e32 v100, v98
	v_mov_b32_e32 v101, v99
	v_mov_b32_e32 v104, v102
	v_mov_b32_e32 v105, v103
	s_cselect_b32 s25, s24, -1
	v_permlane32_swap_b32_e32 v90, v92
	v_permlane32_swap_b32_e32 v91, v93
	v_permlane32_swap_b32_e32 v94, v96
	v_permlane32_swap_b32_e32 v95, v97
	v_permlane32_swap_b32_e32 v98, v100
	v_permlane32_swap_b32_e32 v99, v101
	v_permlane32_swap_b32_e32 v102, v104
	v_permlane32_swap_b32_e32 v103, v105
	s_cmp_lt_i32 s25, 0
	s_mov_b32 s26, s36
	s_mov_b32 s27, s35
	s_cbranch_scc1 .LBB0_118
	s_lshl_b32 s0, s25, 5
	s_add_i32 s37, s0, 0x14400
	v_mov_b32_e32 v2, s37
	ds_read_b128 v[8:11], v2
	v_add_u32_e32 v2, s0, v111
	ds_read2_b32 v[14:15], v2 offset1:4
	v_mov_b32_e32 v6, v62
	v_mov_b32_e32 v7, v62
	s_waitcnt lgkmcnt(1)
	v_readfirstlane_b32 s27, v8
	v_readfirstlane_b32 s26, v9
	v_mov_b32_e32 v8, v62
	v_mov_b32_e32 v9, v62
	v_mov_b64_e32 v[2:3], v[6:7]
	v_mov_b64_e32 v[4:5], v[8:9]
	s_and_saveexec_b64 s[0:1], s[16:17]
	s_cbranch_execz .LBB0_81
	v_mov_b32_e32 v2, s37
	ds_read_b32 v2, v2 offset:16
	v_mov_b32_e32 v3, v62
	s_waitcnt lgkmcnt(0)
	v_cndmask_b32_e64 v2, v2, v11, s[12:13]
	v_cndmask_b32_e64 v2, v2, v10, s[14:15]
	v_lshl_or_b32 v2, v2, 8, v107
	v_lshl_add_u64 v[2:3], v[0:1], 0, v[2:3]
	global_load_dwordx4 v[2:5], v[2:3], off sc0 nt

.LBB0_85:
	s_or_b64 exec, exec, s[0:1]
	s_lshl_b32 s0, s25, 8
	v_add_u32_e32 v70, s0, v113
	ds_read_b128 v[28:31], v70
	s_waitcnt lgkmcnt(1)
	v_mov_b64_e32 v[14:15], v[62:63]
	v_cmp_gt_i32_e32 vcc, s27, v106
	v_mov_b64_e32 v[16:17], v[64:65]
	s_and_saveexec_b64 s[0:1], vcc
	s_cbranch_execz .LBB0_87
	s_waitcnt lgkmcnt(0)
	v_lshl_or_b32 v14, v28, 8, v107
	global_load_dwordx4 v[14:17], v14, s[28:29] sc0 nt
.LBB0_87:
	s_or_b64 exec, exec, s[0:1]
	v_mov_b32_e32 v63, v62
	v_mov_b32_e32 v64, v62
	v_mov_b32_e32 v65, v62
	v_mov_b64_e32 v[18:19], v[62:63]
	v_cmp_gt_i32_e32 vcc, s27, v112
	v_mov_b64_e32 v[20:21], v[64:65]
	s_and_saveexec_b64 s[0:1], vcc
	s_cbranch_execz .LBB0_89
	s_waitcnt lgkmcnt(0)
	v_lshl_or_b32 v18, v29, 8, v107
	global_load_dwordx4 v[18:21], v18, s[28:29] sc0 nt
.LBB0_89:
	s_or_b64 exec, exec, s[0:1]
	v_or_b32_e32 v22, 8, v106
	v_cmp_gt_i32_e32 vcc, s27, v22
	v_mov_b64_e32 v[22:23], v[62:63]
	v_mov_b64_e32 v[24:25], v[64:65]
	s_and_saveexec_b64 s[0:1], vcc
	s_cbranch_execz .LBB0_91
	s_waitcnt lgkmcnt(0)
	v_lshl_or_b32 v22, v30, 8, v107
	global_load_dwordx4 v[22:25], v22, s[28:29] sc0 nt
.LBB0_91:
	s_or_b64 exec, exec, s[0:1]
	v_or_b32_e32 v26, 12, v106
	v_mov_b32_e32 v63, v62
	v_cmp_gt_i32_e32 vcc, s27, v26
	v_mov_b32_e32 v64, v62
	v_mov_b32_e32 v65, v62
	s_waitcnt lgkmcnt(0)
	v_mov_b64_e32 v[26:27], v[62:63]
	v_mov_b64_e32 v[28:29], v[64:65]
	s_and_saveexec_b64 s[0:1], vcc
	s_cbranch_execz .LBB0_93
	v_lshl_or_b32 v26, v31, 8, v107
	global_load_dwordx4 v[26:29], v26, s[28:29] sc0 nt
.LBB0_93:
	s_or_b64 exec, exec, s[0:1]
	ds_read_b128 v[44:47], v70 offset:16
	v_or_b32_e32 v30, 16, v106
	v_cmp_gt_i32_e32 vcc, s27, v30
	v_mov_b64_e32 v[30:31], v[62:63]
	v_mov_b64_e32 v[32:33], v[64:65]
	s_and_saveexec_b64 s[0:1], vcc
	s_cbranch_execz .LBB0_95
	s_waitcnt lgkmcnt(0)
	v_lshl_or_b32 v30, v44, 8, v107
	global_load_dwordx4 v[30:33], v30, s[28:29] sc0 nt
.LBB0_95:
	s_or_b64 exec, exec, s[0:1]
	v_or_b32_e32 v34, 20, v106
	v_mov_b32_e32 v63, v62
	v_cmp_gt_i32_e32 vcc, s27, v34
	v_mov_b32_e32 v64, v62
	v_mov_b32_e32 v65, v62
	v_mov_b64_e32 v[34:35], v[62:63]
	v_mov_b64_e32 v[36:37], v[64:65]
	s_and_saveexec_b64 s[0:1], vcc
	s_cbranch_execz .LBB0_97
	s_waitcnt lgkmcnt(0)
	v_lshl_or_b32 v34, v45, 8, v107
	global_load_dwordx4 v[34:37], v34, s[28:29] sc0 nt
.LBB0_97:
	s_or_b64 exec, exec, s[0:1]
	v_or_b32_e32 v38, 24, v106
	v_cmp_gt_i32_e32 vcc, s27, v38
	v_mov_b64_e32 v[38:39], v[62:63]
	v_mov_b64_e32 v[40:41], v[64:65]
	s_and_saveexec_b64 s[0:1], vcc
	s_cbranch_execz .LBB0_99
	s_waitcnt lgkmcnt(0)
	v_lshl_or_b32 v38, v46, 8, v107
	global_load_dwordx4 v[38:41], v38, s[28:29] sc0 nt
.LBB0_99:
	s_or_b64 exec, exec, s[0:1]
	v_or_b32_e32 v42, 28, v106
	v_mov_b32_e32 v63, v62
	v_cmp_gt_i32_e32 vcc, s27, v42
	v_mov_b32_e32 v64, v62
	v_mov_b32_e32 v65, v62
	s_waitcnt lgkmcnt(0)
	v_mov_b64_e32 v[42:43], v[62:63]
	v_mov_b64_e32 v[44:45], v[64:65]
	s_and_saveexec_b64 s[0:1], vcc
	s_cbranch_execz .LBB0_101
	v_lshl_or_b32 v42, v47, 8, v107
	global_load_dwordx4 v[42:45], v42, s[28:29] sc0 nt
.LBB0_101:
	s_or_b64 exec, exec, s[0:1]
	ds_read_b128 v[66:69], v70 offset:32
	v_or_b32_e32 v46, 32, v106
	v_cmp_gt_i32_e32 vcc, s27, v46
	v_mov_b64_e32 v[46:47], v[62:63]
	v_mov_b64_e32 v[48:49], v[64:65]
	s_and_saveexec_b64 s[0:1], vcc
	s_cbranch_execz .LBB0_103
	s_waitcnt lgkmcnt(0)
	v_lshl_or_b32 v46, v66, 8, v107
	global_load_dwordx4 v[46:49], v46, s[28:29] sc0 nt
.LBB0_103:
	s_or_b64 exec, exec, s[0:1]
	v_or_b32_e32 v50, 36, v106
	v_mov_b32_e32 v63, v62
	v_cmp_gt_i32_e32 vcc, s27, v50
	v_mov_b32_e32 v64, v62
	v_mov_b32_e32 v65, v62
	v_mov_b64_e32 v[50:51], v[62:63]
	v_mov_b64_e32 v[52:53], v[64:65]
	s_and_saveexec_b64 s[0:1], vcc
	s_cbranch_execz .LBB0_105
	s_waitcnt lgkmcnt(0)
	v_lshl_or_b32 v50, v67, 8, v107
	global_load_dwordx4 v[50:53], v50, s[28:29] sc0 nt
.LBB0_105:
	s_or_b64 exec, exec, s[0:1]
	v_or_b32_e32 v54, 40, v106
	v_cmp_gt_i32_e32 vcc, s27, v54
	v_mov_b64_e32 v[54:55], v[62:63]
	v_mov_b64_e32 v[56:57], v[64:65]
	s_and_saveexec_b64 s[0:1], vcc
	s_cbranch_execz .LBB0_107
	s_waitcnt lgkmcnt(0)
	v_lshl_or_b32 v54, v68, 8, v107
	global_load_dwordx4 v[54:57], v54, s[28:29] sc0 nt
.LBB0_107:
	s_or_b64 exec, exec, s[0:1]
	v_or_b32_e32 v58, 44, v106
	v_mov_b32_e32 v63, v62
	v_cmp_gt_i32_e32 vcc, s27, v58
	v_mov_b32_e32 v64, v62
	v_mov_b32_e32 v65, v62
	v_mov_b64_e32 v[58:59], v[62:63]
	v_mov_b64_e32 v[60:61], v[64:65]
	s_and_saveexec_b64 s[0:1], vcc
	s_cbranch_execz .LBB0_109
	s_waitcnt lgkmcnt(0)
	v_lshl_or_b32 v58, v69, 8, v107
	global_load_dwordx4 v[58:61], v58, s[28:29] sc0 nt
.LBB0_109:
	s_or_b64 exec, exec, s[0:1]
	ds_read_b128 v[86:89], v70 offset:48
	s_waitcnt lgkmcnt(1)
	v_or_b32_e32 v66, 48, v106
	v_cmp_gt_i32_e32 vcc, s27, v66
	v_mov_b64_e32 v[68:69], v[64:65]
	v_mov_b64_e32 v[66:67], v[62:63]
	s_and_saveexec_b64 s[0:1], vcc
	s_cbranch_execz .LBB0_111
	s_waitcnt lgkmcnt(0)
	v_lshl_or_b32 v63, v86, 8, v107
	global_load_dwordx4 v[66:69], v63, s[28:29] sc0 nt
.LBB0_111:
	s_or_b64 exec, exec, s[0:1]
	v_or_b32_e32 v63, 52, v106
	v_mov_b32_e32 v64, v62
	v_mov_b32_e32 v65, v62
	v_cmp_gt_i32_e32 vcc, s27, v63
	v_mov_b32_e32 v63, v62
	v_mov_b64_e32 v[72:73], v[64:65]
	v_mov_b64_e32 v[70:71], v[62:63]
	s_and_saveexec_b64 s[0:1], vcc
	s_cbranch_execz .LBB0_113
	s_waitcnt lgkmcnt(0)
	v_lshl_or_b32 v70, v87, 8, v107
	global_load_dwordx4 v[70:73], v70, s[28:29] sc0 nt
.LBB0_113:
	s_or_b64 exec, exec, s[0:1]
	v_or_b32_e32 v74, 56, v106
	v_cmp_gt_i32_e32 vcc, s27, v74
	v_mov_b64_e32 v[76:77], v[64:65]
	v_mov_b64_e32 v[74:75], v[62:63]
	s_and_saveexec_b64 s[0:1], vcc
	s_cbranch_execz .LBB0_115
	s_waitcnt lgkmcnt(0)
	v_lshl_or_b32 v63, v88, 8, v107
	global_load_dwordx4 v[74:77], v63, s[28:29] sc0 nt
.LBB0_115:
	s_or_b64 exec, exec, s[0:1]
	v_mov_b32_e32 v64, v62
	v_mov_b32_e32 v65, v62
	v_mov_b32_e32 v63, v62
	v_mov_b64_e32 v[80:81], v[64:65]
	v_cmp_gt_i32_e32 vcc, s27, v116
	v_mov_b64_e32 v[78:79], v[62:63]
	s_and_saveexec_b64 s[0:1], vcc
	s_cbranch_execz .LBB0_117
	s_waitcnt lgkmcnt(0)
	v_lshl_or_b32 v63, v89, 8, v107
	global_load_dwordx4 v[78:81], v63, s[28:29] sc0 nt
